# v29 with the GLA combine loop at 8 items per group (shorter pipeline tail), alignment-matched
# baseline (speedup 1.0000x reference)
.LBB0_626:
	s_cmp_lt_i32 s90, 6
	s_cselect_b64 s[2:3], -1, 0
	s_and_b64 s[2:3], s[2:3], s[0:1]
	s_andn2_b64 vcc, exec, s[2:3]
	s_cbranch_vccnz .LBB0_653
	s_waitcnt lgkmcnt(0)
	s_add_u32 s20, s88, 0x1ea00000
	s_addc_u32 s21, s89, 0
	s_lshl_b32 s6, s94, 3
	s_add_i32 s10, s79, s6
	s_cmp_gt_i32 s10, 0xffff
	s_cbranch_scc1 .LBB0_636
	s_waitcnt vmcnt(0)
	v_lshlrev_b32_e32 v6, 3, v196
	v_lshlrev_b32_e32 v1, 4, v196
	global_load_dwordx4 v[2:5], v1, s[38:39]
	v_mov_b32_e32 v7, 0x358637bd
	s_lshl_b32 s9, s92, 3
	s_lshl_b32 s11, s92, 6
	s_add_u32 s0, s88, 0x37800000
	s_addc_u32 s1, s89, 0
	s_add_u32 s4, s88, 0x3b800000
	s_addc_u32 s5, s89, 0
	s_add_u32 s22, s20, 0x1000
	s_addc_u32 s23, s21, 0
	s_add_u32 s24, s88, 0x2bf00000
	s_addc_u32 s25, s89, 0
	s_mov_b32 s14, s10
	s_min_i32 s15, s14, 0xffff
	s_lshl_b32 s16, s15, 9
	s_lshr_b32 s17, s15, 2
	s_and_b32 s18, s15, 3
	s_mul_i32 s17, s17, 0x3200
	s_lshl_b32 s18, s18, 9
	s_add_i32 s17, s17, s18
	v_add_u32_e32 v224, s16, v6
	v_add_u32_e32 v225, s17, v6
	global_load_dwordx2 v[8:9], v224, s[0:1]
	global_load_dwordx2 v[10:11], v224, s[4:5]
	global_load_dwordx2 v[12:13], v225, s[22:23]
	s_add_i32 s14, s14, s9
	s_min_i32 s15, s14, 0xffff
	s_lshl_b32 s16, s15, 9
	s_lshr_b32 s17, s15, 2
	s_and_b32 s18, s15, 3
	s_mul_i32 s17, s17, 0x3200
	s_lshl_b32 s18, s18, 9
	s_add_i32 s17, s17, s18
	v_add_u32_e32 v226, s16, v6
	v_add_u32_e32 v227, s17, v6
	global_load_dwordx2 v[14:15], v226, s[0:1]
	global_load_dwordx2 v[16:17], v226, s[4:5]
	global_load_dwordx2 v[18:19], v227, s[22:23]
	s_add_i32 s14, s14, s9
	s_min_i32 s15, s14, 0xffff
	s_lshl_b32 s16, s15, 9
	s_lshr_b32 s17, s15, 2
	s_and_b32 s18, s15, 3
	s_mul_i32 s17, s17, 0x3200
	s_lshl_b32 s18, s18, 9
	s_add_i32 s17, s17, s18
	v_add_u32_e32 v224, s16, v6
	v_add_u32_e32 v225, s17, v6
	global_load_dwordx2 v[20:21], v224, s[0:1]
	global_load_dwordx2 v[22:23], v224, s[4:5]
	global_load_dwordx2 v[24:25], v225, s[22:23]
	s_add_i32 s14, s14, s9
	s_min_i32 s15, s14, 0xffff
	s_lshl_b32 s16, s15, 9
	s_lshr_b32 s17, s15, 2
	s_and_b32 s18, s15, 3
	s_mul_i32 s17, s17, 0x3200
	s_lshl_b32 s18, s18, 9
	s_add_i32 s17, s17, s18
	v_add_u32_e32 v226, s16, v6
	v_add_u32_e32 v227, s17, v6
	global_load_dwordx2 v[26:27], v226, s[0:1]
	global_load_dwordx2 v[28:29], v226, s[4:5]
	global_load_dwordx2 v[30:31], v227, s[22:23]
	s_add_i32 s14, s14, s9
	s_min_i32 s15, s14, 0xffff
	s_lshl_b32 s16, s15, 9
	s_lshr_b32 s17, s15, 2
	s_and_b32 s18, s15, 3
	s_mul_i32 s17, s17, 0x3200
	s_lshl_b32 s18, s18, 9
	s_add_i32 s17, s17, s18
	v_add_u32_e32 v224, s16, v6
	v_add_u32_e32 v225, s17, v6
	global_load_dwordx2 v[32:33], v224, s[0:1]
	global_load_dwordx2 v[34:35], v224, s[4:5]
	global_load_dwordx2 v[36:37], v225, s[22:23]
	s_add_i32 s14, s14, s9
	s_min_i32 s15, s14, 0xffff
	s_lshl_b32 s16, s15, 9
	s_lshr_b32 s17, s15, 2
	s_and_b32 s18, s15, 3
	s_mul_i32 s17, s17, 0x3200
	s_lshl_b32 s18, s18, 9
	s_add_i32 s17, s17, s18
	v_add_u32_e32 v226, s16, v6
	v_add_u32_e32 v227, s17, v6
	global_load_dwordx2 v[38:39], v226, s[0:1]
	global_load_dwordx2 v[40:41], v226, s[4:5]
	global_load_dwordx2 v[42:43], v227, s[22:23]
	s_add_i32 s14, s14, s9
	s_min_i32 s15, s14, 0xffff
	s_lshl_b32 s16, s15, 9
	s_lshr_b32 s17, s15, 2
	s_and_b32 s18, s15, 3
	s_mul_i32 s17, s17, 0x3200
	s_lshl_b32 s18, s18, 9
	s_add_i32 s17, s17, s18
	v_add_u32_e32 v224, s16, v6
	v_add_u32_e32 v225, s17, v6
	global_load_dwordx2 v[44:45], v224, s[0:1]
	global_load_dwordx2 v[46:47], v224, s[4:5]
	global_load_dwordx2 v[48:49], v225, s[22:23]
	s_add_i32 s14, s14, s9
	s_min_i32 s15, s14, 0xffff
	s_lshl_b32 s16, s15, 9
	s_lshr_b32 s17, s15, 2
	s_and_b32 s18, s15, 3
	s_mul_i32 s17, s17, 0x3200
	s_lshl_b32 s18, s18, 9
	s_add_i32 s17, s17, s18
	v_add_u32_e32 v226, s16, v6
	v_add_u32_e32 v227, s17, v6
	global_load_dwordx2 v[50:51], v226, s[0:1]
	global_load_dwordx2 v[52:53], v226, s[4:5]
	global_load_dwordx2 v[54:55], v227, s[22:23]
.Lgc_loop:
	s_add_i32 s19, s10, s11
	s_mov_b32 s14, s19
	s_min_i32 s15, s14, 0xffff
	s_lshl_b32 s16, s15, 9
	s_lshr_b32 s17, s15, 2
	s_and_b32 s18, s15, 3
	s_mul_i32 s17, s17, 0x3200
	s_lshl_b32 s18, s18, 9
	s_add_i32 s17, s17, s18
	v_add_u32_e32 v224, s16, v6
	v_add_u32_e32 v225, s17, v6
	global_load_dwordx2 v[104:105], v224, s[0:1]
	global_load_dwordx2 v[106:107], v224, s[4:5]
	global_load_dwordx2 v[108:109], v225, s[22:23]
	s_add_i32 s14, s14, s9
	s_min_i32 s15, s14, 0xffff
	s_lshl_b32 s16, s15, 9
	s_lshr_b32 s17, s15, 2
	s_and_b32 s18, s15, 3
	s_mul_i32 s17, s17, 0x3200
	s_lshl_b32 s18, s18, 9
	s_add_i32 s17, s17, s18
	v_add_u32_e32 v226, s16, v6
	v_add_u32_e32 v227, s17, v6
	global_load_dwordx2 v[110:111], v226, s[0:1]
	global_load_dwordx2 v[112:113], v226, s[4:5]
	global_load_dwordx2 v[114:115], v227, s[22:23]
	s_add_i32 s14, s14, s9
	s_min_i32 s15, s14, 0xffff
	s_lshl_b32 s16, s15, 9
	s_lshr_b32 s17, s15, 2
	s_and_b32 s18, s15, 3
	s_mul_i32 s17, s17, 0x3200
	s_lshl_b32 s18, s18, 9
	s_add_i32 s17, s17, s18
	v_add_u32_e32 v224, s16, v6
	v_add_u32_e32 v225, s17, v6
	global_load_dwordx2 v[116:117], v224, s[0:1]
	global_load_dwordx2 v[118:119], v224, s[4:5]
	global_load_dwordx2 v[120:121], v225, s[22:23]
	s_add_i32 s14, s14, s9
	s_min_i32 s15, s14, 0xffff
	s_lshl_b32 s16, s15, 9
	s_lshr_b32 s17, s15, 2
	s_and_b32 s18, s15, 3
	s_mul_i32 s17, s17, 0x3200
	s_lshl_b32 s18, s18, 9
	s_add_i32 s17, s17, s18
	v_add_u32_e32 v226, s16, v6
	v_add_u32_e32 v227, s17, v6
	global_load_dwordx2 v[122:123], v226, s[0:1]
	global_load_dwordx2 v[124:125], v226, s[4:5]
	global_load_dwordx2 v[126:127], v227, s[22:23]
	s_add_i32 s14, s14, s9
	s_min_i32 s15, s14, 0xffff
	s_lshl_b32 s16, s15, 9
	s_lshr_b32 s17, s15, 2
	s_and_b32 s18, s15, 3
	s_mul_i32 s17, s17, 0x3200
	s_lshl_b32 s18, s18, 9
	s_add_i32 s17, s17, s18
	v_add_u32_e32 v224, s16, v6
	v_add_u32_e32 v225, s17, v6
	global_load_dwordx2 v[128:129], v224, s[0:1]
	global_load_dwordx2 v[130:131], v224, s[4:5]
	global_load_dwordx2 v[132:133], v225, s[22:23]
	s_add_i32 s14, s14, s9
	s_min_i32 s15, s14, 0xffff
	s_lshl_b32 s16, s15, 9
	s_lshr_b32 s17, s15, 2
	s_and_b32 s18, s15, 3
	s_mul_i32 s17, s17, 0x3200
	s_lshl_b32 s18, s18, 9
	s_add_i32 s17, s17, s18
	v_add_u32_e32 v226, s16, v6
	v_add_u32_e32 v227, s17, v6
	global_load_dwordx2 v[134:135], v226, s[0:1]
	global_load_dwordx2 v[136:137], v226, s[4:5]
	global_load_dwordx2 v[138:139], v227, s[22:23]
	s_add_i32 s14, s14, s9
	s_min_i32 s15, s14, 0xffff
	s_lshl_b32 s16, s15, 9
	s_lshr_b32 s17, s15, 2
	s_and_b32 s18, s15, 3
	s_mul_i32 s17, s17, 0x3200
	s_lshl_b32 s18, s18, 9
	s_add_i32 s17, s17, s18
	v_add_u32_e32 v224, s16, v6
	v_add_u32_e32 v225, s17, v6
	global_load_dwordx2 v[140:141], v224, s[0:1]
	global_load_dwordx2 v[142:143], v224, s[4:5]
	global_load_dwordx2 v[144:145], v225, s[22:23]
	s_add_i32 s14, s14, s9
	s_min_i32 s15, s14, 0xffff
	s_lshl_b32 s16, s15, 9
	s_lshr_b32 s17, s15, 2
	s_and_b32 s18, s15, 3
	s_mul_i32 s17, s17, 0x3200
	s_lshl_b32 s18, s18, 9
	s_add_i32 s17, s17, s18
	v_add_u32_e32 v226, s16, v6
	v_add_u32_e32 v227, s17, v6
	global_load_dwordx2 v[146:147], v226, s[0:1]
	global_load_dwordx2 v[148:149], v226, s[4:5]
	global_load_dwordx2 v[150:151], v227, s[22:23]
	s_waitcnt vmcnt(24)
	s_mov_b32 s14, s10
	v_lshlrev_b32_e32 v204, 16, v8
	v_lshlrev_b32_e32 v224, 16, v10
	v_and_b32_e32 v205, 0xffff0000, v8
	v_and_b32_e32 v225, 0xffff0000, v10
	v_add_f32_e32 v204, v204, v224
	v_add_f32_e32 v205, v205, v225
	v_lshlrev_b32_e32 v206, 16, v9
	v_lshlrev_b32_e32 v224, 16, v11
	v_and_b32_e32 v207, 0xffff0000, v9
	v_and_b32_e32 v225, 0xffff0000, v11
	v_add_f32_e32 v206, v206, v224
	v_add_f32_e32 v207, v207, v225
	v_mul_f32_e32 v224, v204, v204
	v_mul_f32_e32 v225, v205, v205
	v_add_f32_e32 v220, v224, v225
	v_mul_f32_e32 v224, v206, v206
	v_mul_f32_e32 v225, v207, v207
	v_add_f32_e32 v220, v224, v220
	v_add_f32_e32 v220, v225, v220
	v_lshlrev_b32_e32 v208, 16, v14
	v_lshlrev_b32_e32 v226, 16, v16
	v_and_b32_e32 v209, 0xffff0000, v14
	v_and_b32_e32 v227, 0xffff0000, v16
	v_add_f32_e32 v208, v208, v226
	v_add_f32_e32 v209, v209, v227
	v_lshlrev_b32_e32 v210, 16, v15
	v_lshlrev_b32_e32 v226, 16, v17
	v_and_b32_e32 v211, 0xffff0000, v15
	v_and_b32_e32 v227, 0xffff0000, v17
	v_add_f32_e32 v210, v210, v226
	v_add_f32_e32 v211, v211, v227
	v_mul_f32_e32 v226, v208, v208
	v_mul_f32_e32 v227, v209, v209
	v_add_f32_e32 v221, v226, v227
	v_mul_f32_e32 v226, v210, v210
	v_mul_f32_e32 v227, v211, v211
	v_add_f32_e32 v221, v226, v221
	v_add_f32_e32 v221, v227, v221
	v_lshlrev_b32_e32 v212, 16, v20
	v_lshlrev_b32_e32 v224, 16, v22
	v_and_b32_e32 v213, 0xffff0000, v20
	v_and_b32_e32 v225, 0xffff0000, v22
	v_add_f32_e32 v212, v212, v224
	v_add_f32_e32 v213, v213, v225
	v_lshlrev_b32_e32 v214, 16, v21
	v_lshlrev_b32_e32 v224, 16, v23
	v_and_b32_e32 v215, 0xffff0000, v21
	v_and_b32_e32 v225, 0xffff0000, v23
	v_add_f32_e32 v214, v214, v224
	v_add_f32_e32 v215, v215, v225
	v_mul_f32_e32 v224, v212, v212
	v_mul_f32_e32 v225, v213, v213
	v_add_f32_e32 v222, v224, v225
	v_mul_f32_e32 v224, v214, v214
	v_mul_f32_e32 v225, v215, v215
	v_add_f32_e32 v222, v224, v222
	v_add_f32_e32 v222, v225, v222
	v_lshlrev_b32_e32 v216, 16, v26
	v_lshlrev_b32_e32 v226, 16, v28
	v_and_b32_e32 v217, 0xffff0000, v26
	v_and_b32_e32 v227, 0xffff0000, v28
	v_add_f32_e32 v216, v216, v226
	v_add_f32_e32 v217, v217, v227
	v_lshlrev_b32_e32 v218, 16, v27
	v_lshlrev_b32_e32 v226, 16, v29
	v_and_b32_e32 v219, 0xffff0000, v27
	v_and_b32_e32 v227, 0xffff0000, v29
	v_add_f32_e32 v218, v218, v226
	v_add_f32_e32 v219, v219, v227
	v_mul_f32_e32 v226, v216, v216
	v_mul_f32_e32 v227, v217, v217
	v_add_f32_e32 v223, v226, v227
	v_mul_f32_e32 v226, v218, v218
	v_mul_f32_e32 v227, v219, v219
	v_add_f32_e32 v223, v226, v223
	v_add_f32_e32 v223, v227, v223
	v_mov_b32_e32 v224, v220
	v_mov_b32_e32 v225, v221
	v_mov_b32_e32 v226, v222
	v_mov_b32_e32 v227, v223
	v_permlane32_swap_b32_e32 v220, v224
	v_permlane32_swap_b32_e32 v221, v225
	v_permlane32_swap_b32_e32 v222, v226
	v_permlane32_swap_b32_e32 v223, v227
	v_add_f32_e32 v220, v220, v224
	v_add_f32_e32 v221, v221, v225
	v_add_f32_e32 v222, v222, v226
	v_add_f32_e32 v223, v223, v227
	v_mov_b32_e32 v224, v220
	v_mov_b32_e32 v225, v221
	v_mov_b32_e32 v226, v222
	v_mov_b32_e32 v227, v223
	v_permlane16_swap_b32_e32 v220, v224
	v_permlane16_swap_b32_e32 v221, v225
	v_permlane16_swap_b32_e32 v222, v226
	v_permlane16_swap_b32_e32 v223, v227
	v_add_f32_e32 v220, v220, v224
	v_add_f32_e32 v221, v221, v225
	v_add_f32_e32 v222, v222, v226
	v_add_f32_e32 v223, v223, v227
	v_add_f32_dpp v220, v220, v220 row_ror:8 row_mask:0xf bank_mask:0xf
	v_add_f32_dpp v221, v221, v221 row_ror:8 row_mask:0xf bank_mask:0xf
	v_add_f32_dpp v222, v222, v222 row_ror:8 row_mask:0xf bank_mask:0xf
	v_add_f32_dpp v223, v223, v223 row_ror:8 row_mask:0xf bank_mask:0xf
	v_add_f32_dpp v220, v220, v220 row_ror:4 row_mask:0xf bank_mask:0xf
	v_add_f32_dpp v221, v221, v221 row_ror:4 row_mask:0xf bank_mask:0xf
	v_add_f32_dpp v222, v222, v222 row_ror:4 row_mask:0xf bank_mask:0xf
	v_add_f32_dpp v223, v223, v223 row_ror:4 row_mask:0xf bank_mask:0xf
	v_add_f32_dpp v220, v220, v220 row_ror:2 row_mask:0xf bank_mask:0xf
	v_add_f32_dpp v221, v221, v221 row_ror:2 row_mask:0xf bank_mask:0xf
	v_add_f32_dpp v222, v222, v222 row_ror:2 row_mask:0xf bank_mask:0xf
	v_add_f32_dpp v223, v223, v223 row_ror:2 row_mask:0xf bank_mask:0xf
	v_add_f32_dpp v220, v220, v220 row_ror:1 row_mask:0xf bank_mask:0xf
	v_add_f32_dpp v221, v221, v221 row_ror:1 row_mask:0xf bank_mask:0xf
	v_add_f32_dpp v222, v222, v222 row_ror:1 row_mask:0xf bank_mask:0xf
	v_add_f32_dpp v223, v223, v223 row_ror:1 row_mask:0xf bank_mask:0xf
	v_fmamk_f32 v226, v220, 0x3b800000, v7
	v_rsq_f32_e32 v226, v226
	v_lshlrev_b32_e32 v224, 16, v12
	v_lshlrev_b32_e32 v225, 16, v13
	v_mul_f32_e32 v204, v204, v226
	v_mul_f32_e32 v205, v205, v226
	v_mul_f32_e32 v206, v206, v226
	v_mul_f32_e32 v207, v207, v226
	v_mul_f32_e32 v204, v2, v204
	v_mul_f32_e32 v205, v3, v205
	v_mul_f32_e32 v206, v4, v206
	v_mul_f32_e32 v207, v5, v207
	v_and_b32_e32 v12, 0xffff0000, v12
	v_and_b32_e32 v13, 0xffff0000, v13
	v_mul_f32_e32 v226, 0xbfb8aa3b, v224
	v_mul_f32_e32 v227, 0xbfb8aa3b, v12
	v_mul_f32_e32 v1, 0xbfb8aa3b, v225
	v_mul_f32_e32 v220, 0xbfb8aa3b, v13
	v_exp_f32_e32 v226, v226
	v_exp_f32_e32 v227, v227
	v_exp_f32_e32 v1, v1
	v_exp_f32_e32 v220, v220
	v_add_f32_e32 v226, 1.0, v226
	v_add_f32_e32 v227, 1.0, v227
	v_add_f32_e32 v1, 1.0, v1
	v_add_f32_e32 v220, 1.0, v220
	v_rcp_f32_e32 v226, v226
	v_rcp_f32_e32 v227, v227
	v_rcp_f32_e32 v1, v1
	v_rcp_f32_e32 v220, v220
	v_mul_f32_e32 v224, v226, v224
	v_mul_f32_e32 v12, v227, v12
	v_mul_f32_e32 v225, v1, v225
	v_mul_f32_e32 v13, v220, v13
	v_mul_f32_e32 v204, v224, v204
	v_mul_f32_e32 v205, v12, v205
	v_mul_f32_e32 v206, v225, v206
	v_mul_f32_e32 v207, v13, v207
	v_cvt_pk_bf16_f32 v224, v204, v205
	v_cvt_pk_bf16_f32 v225, v206, v207
	s_cmp_gt_i32 s14, 0xffff
	s_cbranch_scc1 .Lgc_skip_a_0
	s_lshr_b32 s17, s14, 2
	s_and_b32 s18, s14, 3
	s_lshl_b32 s17, s17, 12
	s_lshl_b32 s18, s18, 9
	s_add_i32 s17, s17, s18
	v_add_u32_e32 v227, s17, v6
	global_store_dwordx2 v227, v[224:225], s[24:25]

.Lgc_skip_a_7:
	s_mov_b32 s10, s19
	s_cmp_gt_i32 s10, 0xffff
	s_cbranch_scc1 .Lgc_done
	s_add_i32 s19, s10, s11
	s_mov_b32 s14, s19
	s_min_i32 s15, s14, 0xffff
	s_lshl_b32 s16, s15, 9
	s_lshr_b32 s17, s15, 2
	s_and_b32 s18, s15, 3
	s_mul_i32 s17, s17, 0x3200
	s_lshl_b32 s18, s18, 9
	s_add_i32 s17, s17, s18
	v_add_u32_e32 v224, s16, v6
	v_add_u32_e32 v225, s17, v6
	global_load_dwordx2 v[8:9], v224, s[0:1]
	global_load_dwordx2 v[10:11], v224, s[4:5]
	global_load_dwordx2 v[12:13], v225, s[22:23]
	s_add_i32 s14, s14, s9
	s_min_i32 s15, s14, 0xffff
	s_lshl_b32 s16, s15, 9
	s_lshr_b32 s17, s15, 2
	s_and_b32 s18, s15, 3
	s_mul_i32 s17, s17, 0x3200
	s_lshl_b32 s18, s18, 9
	s_add_i32 s17, s17, s18
	v_add_u32_e32 v226, s16, v6
	v_add_u32_e32 v227, s17, v6
	global_load_dwordx2 v[14:15], v226, s[0:1]
	global_load_dwordx2 v[16:17], v226, s[4:5]
	global_load_dwordx2 v[18:19], v227, s[22:23]
	s_add_i32 s14, s14, s9
	s_min_i32 s15, s14, 0xffff
	s_lshl_b32 s16, s15, 9
	s_lshr_b32 s17, s15, 2
	s_and_b32 s18, s15, 3
	s_mul_i32 s17, s17, 0x3200
	s_lshl_b32 s18, s18, 9
	s_add_i32 s17, s17, s18
	v_add_u32_e32 v224, s16, v6
	v_add_u32_e32 v225, s17, v6
	global_load_dwordx2 v[20:21], v224, s[0:1]
	global_load_dwordx2 v[22:23], v224, s[4:5]
	global_load_dwordx2 v[24:25], v225, s[22:23]
	s_add_i32 s14, s14, s9
	s_min_i32 s15, s14, 0xffff
	s_lshl_b32 s16, s15, 9
	s_lshr_b32 s17, s15, 2
	s_and_b32 s18, s15, 3
	s_mul_i32 s17, s17, 0x3200
	s_lshl_b32 s18, s18, 9
	s_add_i32 s17, s17, s18
	v_add_u32_e32 v226, s16, v6
	v_add_u32_e32 v227, s17, v6
	global_load_dwordx2 v[26:27], v226, s[0:1]
	global_load_dwordx2 v[28:29], v226, s[4:5]
	global_load_dwordx2 v[30:31], v227, s[22:23]
	s_add_i32 s14, s14, s9
	s_min_i32 s15, s14, 0xffff
	s_lshl_b32 s16, s15, 9
	s_lshr_b32 s17, s15, 2
	s_and_b32 s18, s15, 3
	s_mul_i32 s17, s17, 0x3200
	s_lshl_b32 s18, s18, 9
	s_add_i32 s17, s17, s18
	v_add_u32_e32 v224, s16, v6
	v_add_u32_e32 v225, s17, v6
	global_load_dwordx2 v[32:33], v224, s[0:1]
	global_load_dwordx2 v[34:35], v224, s[4:5]
	global_load_dwordx2 v[36:37], v225, s[22:23]
	s_add_i32 s14, s14, s9
	s_min_i32 s15, s14, 0xffff
	s_lshl_b32 s16, s15, 9
	s_lshr_b32 s17, s15, 2
	s_and_b32 s18, s15, 3
	s_mul_i32 s17, s17, 0x3200
	s_lshl_b32 s18, s18, 9
	s_add_i32 s17, s17, s18
	v_add_u32_e32 v226, s16, v6
	v_add_u32_e32 v227, s17, v6
	global_load_dwordx2 v[38:39], v226, s[0:1]
	global_load_dwordx2 v[40:41], v226, s[4:5]
	global_load_dwordx2 v[42:43], v227, s[22:23]
	s_add_i32 s14, s14, s9
	s_min_i32 s15, s14, 0xffff
	s_lshl_b32 s16, s15, 9
	s_lshr_b32 s17, s15, 2
	s_and_b32 s18, s15, 3
	s_mul_i32 s17, s17, 0x3200
	s_lshl_b32 s18, s18, 9
	s_add_i32 s17, s17, s18
	v_add_u32_e32 v224, s16, v6
	v_add_u32_e32 v225, s17, v6
	global_load_dwordx2 v[44:45], v224, s[0:1]
	global_load_dwordx2 v[46:47], v224, s[4:5]
	global_load_dwordx2 v[48:49], v225, s[22:23]
	s_add_i32 s14, s14, s9
	s_min_i32 s15, s14, 0xffff
	s_lshl_b32 s16, s15, 9
	s_lshr_b32 s17, s15, 2
	s_and_b32 s18, s15, 3
	s_mul_i32 s17, s17, 0x3200
	s_lshl_b32 s18, s18, 9
	s_add_i32 s17, s17, s18
	v_add_u32_e32 v226, s16, v6
	v_add_u32_e32 v227, s17, v6
	global_load_dwordx2 v[50:51], v226, s[0:1]
	global_load_dwordx2 v[52:53], v226, s[4:5]
	global_load_dwordx2 v[54:55], v227, s[22:23]
	s_waitcnt vmcnt(24)
	s_mov_b32 s14, s10
	v_lshlrev_b32_e32 v204, 16, v104
	v_lshlrev_b32_e32 v224, 16, v106
	v_and_b32_e32 v205, 0xffff0000, v104
	v_and_b32_e32 v225, 0xffff0000, v106
	v_add_f32_e32 v204, v204, v224
	v_add_f32_e32 v205, v205, v225
	v_lshlrev_b32_e32 v206, 16, v105
	v_lshlrev_b32_e32 v224, 16, v107
	v_and_b32_e32 v207, 0xffff0000, v105
	v_and_b32_e32 v225, 0xffff0000, v107
	v_add_f32_e32 v206, v206, v224
	v_add_f32_e32 v207, v207, v225
	v_mul_f32_e32 v224, v204, v204
	v_mul_f32_e32 v225, v205, v205
	v_add_f32_e32 v220, v224, v225
	v_mul_f32_e32 v224, v206, v206
	v_mul_f32_e32 v225, v207, v207
	v_add_f32_e32 v220, v224, v220
	v_add_f32_e32 v220, v225, v220
	v_lshlrev_b32_e32 v208, 16, v110
	v_lshlrev_b32_e32 v226, 16, v112
	v_and_b32_e32 v209, 0xffff0000, v110
	v_and_b32_e32 v227, 0xffff0000, v112
	v_add_f32_e32 v208, v208, v226
	v_add_f32_e32 v209, v209, v227
	v_lshlrev_b32_e32 v210, 16, v111
	v_lshlrev_b32_e32 v226, 16, v113
	v_and_b32_e32 v211, 0xffff0000, v111
	v_and_b32_e32 v227, 0xffff0000, v113
	v_add_f32_e32 v210, v210, v226
	v_add_f32_e32 v211, v211, v227
	v_mul_f32_e32 v226, v208, v208
	v_mul_f32_e32 v227, v209, v209
	v_add_f32_e32 v221, v226, v227
	v_mul_f32_e32 v226, v210, v210
	v_mul_f32_e32 v227, v211, v211
	v_add_f32_e32 v221, v226, v221
	v_add_f32_e32 v221, v227, v221
	v_lshlrev_b32_e32 v212, 16, v116
	v_lshlrev_b32_e32 v224, 16, v118
	v_and_b32_e32 v213, 0xffff0000, v116
	v_and_b32_e32 v225, 0xffff0000, v118
	v_add_f32_e32 v212, v212, v224
	v_add_f32_e32 v213, v213, v225
	v_lshlrev_b32_e32 v214, 16, v117
	v_lshlrev_b32_e32 v224, 16, v119
	v_and_b32_e32 v215, 0xffff0000, v117
	v_and_b32_e32 v225, 0xffff0000, v119
	v_add_f32_e32 v214, v214, v224
	v_add_f32_e32 v215, v215, v225
	v_mul_f32_e32 v224, v212, v212
	v_mul_f32_e32 v225, v213, v213
	v_add_f32_e32 v222, v224, v225
	v_mul_f32_e32 v224, v214, v214
	v_mul_f32_e32 v225, v215, v215
	v_add_f32_e32 v222, v224, v222
	v_add_f32_e32 v222, v225, v222
	v_lshlrev_b32_e32 v216, 16, v122
	v_lshlrev_b32_e32 v226, 16, v124
	v_and_b32_e32 v217, 0xffff0000, v122
	v_and_b32_e32 v227, 0xffff0000, v124
	v_add_f32_e32 v216, v216, v226
	v_add_f32_e32 v217, v217, v227
	v_lshlrev_b32_e32 v218, 16, v123
	v_lshlrev_b32_e32 v226, 16, v125
	v_and_b32_e32 v219, 0xffff0000, v123
	v_and_b32_e32 v227, 0xffff0000, v125
	v_add_f32_e32 v218, v218, v226
	v_add_f32_e32 v219, v219, v227
	v_mul_f32_e32 v226, v216, v216
	v_mul_f32_e32 v227, v217, v217
	v_add_f32_e32 v223, v226, v227
	v_mul_f32_e32 v226, v218, v218
	v_mul_f32_e32 v227, v219, v219
	v_add_f32_e32 v223, v226, v223
	v_add_f32_e32 v223, v227, v223
	v_mov_b32_e32 v224, v220
	v_mov_b32_e32 v225, v221
	v_mov_b32_e32 v226, v222
	v_mov_b32_e32 v227, v223
	v_permlane32_swap_b32_e32 v220, v224
	v_permlane32_swap_b32_e32 v221, v225
	v_permlane32_swap_b32_e32 v222, v226
	v_permlane32_swap_b32_e32 v223, v227
	v_add_f32_e32 v220, v220, v224
	v_add_f32_e32 v221, v221, v225
	v_add_f32_e32 v222, v222, v226
	v_add_f32_e32 v223, v223, v227
	v_mov_b32_e32 v224, v220
	v_mov_b32_e32 v225, v221
	v_mov_b32_e32 v226, v222
	v_mov_b32_e32 v227, v223
	v_permlane16_swap_b32_e32 v220, v224
	v_permlane16_swap_b32_e32 v221, v225
	v_permlane16_swap_b32_e32 v222, v226
	v_permlane16_swap_b32_e32 v223, v227
	v_add_f32_e32 v220, v220, v224
	v_add_f32_e32 v221, v221, v225
	v_add_f32_e32 v222, v222, v226
	v_add_f32_e32 v223, v223, v227
	v_add_f32_dpp v220, v220, v220 row_ror:8 row_mask:0xf bank_mask:0xf
	v_add_f32_dpp v221, v221, v221 row_ror:8 row_mask:0xf bank_mask:0xf
	v_add_f32_dpp v222, v222, v222 row_ror:8 row_mask:0xf bank_mask:0xf
	v_add_f32_dpp v223, v223, v223 row_ror:8 row_mask:0xf bank_mask:0xf
	v_add_f32_dpp v220, v220, v220 row_ror:4 row_mask:0xf bank_mask:0xf
	v_add_f32_dpp v221, v221, v221 row_ror:4 row_mask:0xf bank_mask:0xf
	v_add_f32_dpp v222, v222, v222 row_ror:4 row_mask:0xf bank_mask:0xf
	v_add_f32_dpp v223, v223, v223 row_ror:4 row_mask:0xf bank_mask:0xf
	v_add_f32_dpp v220, v220, v220 row_ror:2 row_mask:0xf bank_mask:0xf
	v_add_f32_dpp v221, v221, v221 row_ror:2 row_mask:0xf bank_mask:0xf
	v_add_f32_dpp v222, v222, v222 row_ror:2 row_mask:0xf bank_mask:0xf
	v_add_f32_dpp v223, v223, v223 row_ror:2 row_mask:0xf bank_mask:0xf
	v_add_f32_dpp v220, v220, v220 row_ror:1 row_mask:0xf bank_mask:0xf
	v_add_f32_dpp v221, v221, v221 row_ror:1 row_mask:0xf bank_mask:0xf
	v_add_f32_dpp v222, v222, v222 row_ror:1 row_mask:0xf bank_mask:0xf
	v_add_f32_dpp v223, v223, v223 row_ror:1 row_mask:0xf bank_mask:0xf
	v_fmamk_f32 v226, v220, 0x3b800000, v7
	v_rsq_f32_e32 v226, v226
	v_lshlrev_b32_e32 v224, 16, v108
	v_lshlrev_b32_e32 v225, 16, v109
	v_mul_f32_e32 v204, v204, v226
	v_mul_f32_e32 v205, v205, v226
	v_mul_f32_e32 v206, v206, v226
	v_mul_f32_e32 v207, v207, v226
	v_mul_f32_e32 v204, v2, v204
	v_mul_f32_e32 v205, v3, v205
	v_mul_f32_e32 v206, v4, v206
	v_mul_f32_e32 v207, v5, v207
	v_and_b32_e32 v108, 0xffff0000, v108
	v_and_b32_e32 v109, 0xffff0000, v109
	v_mul_f32_e32 v226, 0xbfb8aa3b, v224
	v_mul_f32_e32 v227, 0xbfb8aa3b, v108
	v_mul_f32_e32 v1, 0xbfb8aa3b, v225
	v_mul_f32_e32 v220, 0xbfb8aa3b, v109
	v_exp_f32_e32 v226, v226
	v_exp_f32_e32 v227, v227
	v_exp_f32_e32 v1, v1
	v_exp_f32_e32 v220, v220
	v_add_f32_e32 v226, 1.0, v226
	v_add_f32_e32 v227, 1.0, v227
	v_add_f32_e32 v1, 1.0, v1
	v_add_f32_e32 v220, 1.0, v220
	v_rcp_f32_e32 v226, v226
	v_rcp_f32_e32 v227, v227
	v_rcp_f32_e32 v1, v1
	v_rcp_f32_e32 v220, v220
	v_mul_f32_e32 v224, v226, v224
	v_mul_f32_e32 v108, v227, v108
	v_mul_f32_e32 v225, v1, v225
	v_mul_f32_e32 v109, v220, v109
	v_mul_f32_e32 v204, v224, v204
	v_mul_f32_e32 v205, v108, v205
	v_mul_f32_e32 v206, v225, v206
	v_mul_f32_e32 v207, v109, v207
	v_cvt_pk_bf16_f32 v224, v204, v205
	v_cvt_pk_bf16_f32 v225, v206, v207
	s_cmp_gt_i32 s14, 0xffff
	s_cbranch_scc1 .Lgc_skip_b_0
	s_lshr_b32 s17, s14, 2
	s_and_b32 s18, s14, 3
	s_lshl_b32 s17, s17, 12
	s_lshl_b32 s18, s18, 9
	s_add_i32 s17, s17, s18
	v_add_u32_e32 v227, s17, v6
	global_store_dwordx2 v227, v[224:225], s[24:25]

.Lgc_skip_b_6:
	s_add_i32 s14, s14, s9
	v_fmamk_f32 v224, v223, 0x3b800000, v7
	v_rsq_f32_e32 v224, v224
	v_lshlrev_b32_e32 v226, 16, v150
	v_lshlrev_b32_e32 v227, 16, v151
	v_mul_f32_e32 v216, v216, v224
	v_mul_f32_e32 v217, v217, v224
	v_mul_f32_e32 v218, v218, v224
	v_mul_f32_e32 v219, v219, v224
	v_mul_f32_e32 v216, v2, v216
	v_mul_f32_e32 v217, v3, v217
	v_mul_f32_e32 v218, v4, v218
	v_mul_f32_e32 v219, v5, v219
	v_and_b32_e32 v150, 0xffff0000, v150
	v_and_b32_e32 v151, 0xffff0000, v151
	v_mul_f32_e32 v224, 0xbfb8aa3b, v226
	v_mul_f32_e32 v225, 0xbfb8aa3b, v150
	v_mul_f32_e32 v1, 0xbfb8aa3b, v227
	v_mul_f32_e32 v223, 0xbfb8aa3b, v151
	v_exp_f32_e32 v224, v224
	v_exp_f32_e32 v225, v225
	v_exp_f32_e32 v1, v1
	v_exp_f32_e32 v223, v223
	v_add_f32_e32 v224, 1.0, v224
	v_add_f32_e32 v225, 1.0, v225
	v_add_f32_e32 v1, 1.0, v1
	v_add_f32_e32 v223, 1.0, v223
	v_rcp_f32_e32 v224, v224
	v_rcp_f32_e32 v225, v225
	v_rcp_f32_e32 v1, v1
	v_rcp_f32_e32 v223, v223
	v_mul_f32_e32 v226, v224, v226
	v_mul_f32_e32 v150, v225, v150
	v_mul_f32_e32 v227, v1, v227
	v_mul_f32_e32 v151, v223, v151
	v_mul_f32_e32 v216, v226, v216
	v_mul_f32_e32 v217, v150, v217
	v_mul_f32_e32 v218, v227, v218
	v_mul_f32_e32 v219, v151, v219
	v_cvt_pk_bf16_f32 v226, v216, v217
	v_cvt_pk_bf16_f32 v227, v218, v219
	s_cmp_gt_i32 s14, 0xffff
	s_cbranch_scc1 .Lgc_skip_b_7
	s_lshr_b32 s17, s14, 2
	s_and_b32 s18, s14, 3
	s_lshl_b32 s17, s17, 12
	s_lshl_b32 s18, s18, 9
	s_add_i32 s17, s17, s18
	v_add_u32_e32 v225, s17, v6
	global_store_dwordx2 v225, v[226:227], s[24:25]
.Lgc_skip_b_7:
	s_mov_b32 s10, s19
	s_cmp_gt_i32 s10, 0xffff
	s_cbranch_scc0 .Lgc_loop
